# baseline (speedup 1.0000x reference)
_Z11sloc_kernelPKDF16_PKfS2_PDF16_:
	s_and_b32 s3, s2, 7
	s_lshr_b32 s2, s2, 3
	s_lshl_b32 s3, s3, 7
	s_or_b32 s2, s2, s3
	s_load_dwordx8 s[4:11], s[0:1], 0x0
	s_ashr_i32 s0, s2, 31
	s_lshr_b32 s1, s0, 28
	s_lshr_b32 s0, s0, 23
	s_add_i32 s0, s2, s0
	s_add_i32 s1, s2, s1
	s_ashr_i32 s18, s0, 9
	s_bfe_u32 s20, s1, 0x50004
	s_ashr_i32 s19, s18, 31
	s_mul_i32 s13, s18, 0x900
	s_mul_hi_i32 s12, s18, 0x900
	s_add_u32 s0, s13, 0x800
	v_lshrrev_b32_e32 v2, 1, v0
	s_addc_u32 s1, s12, 0
	v_and_b32_e32 v41, 0x60, v2
	v_or_b32_e32 v2, s0, v41
	v_mov_b32_e32 v3, s1
	v_lshlrev_b64 v[2:3], 13, v[2:3]
	v_bfe_u32 v1, v0, 4, 2
	s_waitcnt lgkmcnt(0)
	v_lshl_add_u64 v[2:3], s[4:5], 0, v[2:3]
	s_lshl_b32 s0, s20, 8
	s_mov_b32 s1, 0
	v_and_b32_e32 v40, 15, v0
	v_lshl_add_u64 v[2:3], v[2:3], 0, s[0:1]
	v_lshlrev_b32_e32 v46, 4, v1
	v_mov_b32_e32 v47, 0
	v_lshl_add_u64 v[2:3], v[2:3], 0, v[46:47]
	v_lshlrev_b32_e32 v4, 13, v40
	v_mov_b32_e32 v5, v47
	v_lshl_add_u64 v[18:19], v[2:3], 0, v[4:5]
	s_mov_b32 s14, 0x20000
	v_add_co_u32_e32 v34, vcc, s14, v18
	global_load_dwordx4 v[2:5], v[18:19], off
	global_load_dwordx4 v[6:9], v[18:19], off offset:64
	global_load_dwordx4 v[10:13], v[18:19], off offset:128
	global_load_dwordx4 v[14:17], v[18:19], off offset:192
	v_addc_co_u32_e32 v35, vcc, 0, v19, vcc
	global_load_dwordx4 v[18:21], v[34:35], off
	global_load_dwordx4 v[22:25], v[34:35], off offset:64
	global_load_dwordx4 v[26:29], v[34:35], off offset:128
	global_load_dwordx4 v[30:33], v[34:35], off offset:192
	s_lshl_b32 s2, s2, 1
	s_and_b32 s15, s2, 30
	s_lshl_b64 s[2:3], s[18:19], 17
	s_lshl_b32 s16, s20, 9
	s_add_u32 s6, s6, s16
	s_addc_u32 s7, s7, 0
	s_add_u32 s16, s8, s16
	v_lshrrev_b32_e32 v35, 4, v0
	s_addc_u32 s17, s9, 0
	v_lshlrev_b32_e32 v0, 3, v0
	v_and_b32_e32 v34, 0x78, v0
	s_add_u32 s4, s4, s0
	s_addc_u32 s5, s5, 0
	v_lshlrev_b32_e32 v36, 1, v34
	v_mov_b32_e32 v37, v47
	s_lshl_b32 s0, s18, 5
	v_lshl_add_u64 v[38:39], s[4:5], 0, v[36:37]
	s_or_b32 s4, s0, s20
	s_ashr_i32 s5, s4, 31
	s_lshl_b64 s[4:5], s[4:5], 19
	v_lshlrev_b32_e32 v42, 3, v1
	s_add_u32 s4, s10, s4
	v_lshl_or_b32 v41, v41, 1, v42
	s_addc_u32 s5, s11, s5
	v_mul_u32_u24_e32 v52, 0x110, v40
	v_lshlrev_b32_e32 v40, 7, v35
	v_lshlrev_b32_e32 v0, 2, v34
	v_mov_b32_e32 v1, v47
	v_or_b32_e32 v43, 0x4400, v36
	v_or_b32_e32 v45, 0x4400, v46
	v_lshl_add_u64 v[48:49], s[4:5], 0, v[36:37]
	v_mul_u32_u24_e32 v37, 0x110, v35
	v_or_b32_e32 v42, 0x800, v40
	v_or_b32_e32 v44, 0x1000, v40
	v_or_b32_e32 v56, 0x1800, v40
	v_lshlrev_b32_e32 v46, 13, v35
	v_add_u32_e32 v67, v41, v52
	v_lshl_add_u64 v[0:1], s[6:7], 0, v[0:1]
	v_lshl_add_u64 v[50:51], v[38:39], 0, v[46:47]
	s_mov_b64 s[6:7], -1
	s_lshl_b64 s[2:3], s[2:3], 2
	v_lshlrev_b32_e32 v64, 2, v34
	s_mov_b32 s5, 0x40000
	s_mov_b32 s10, 0x60000
	v_add_u32_e32 v65, v43, v37
	v_add_u32_e32 v66, v45, v52
	s_mov_b32 s4, 0x41800000
	v_add_u32_e32 v68, v36, v37
	v_add_u32_e32 v69, 0x1000, v67
	v_add_u32_e32 v70, 0x2000, v67
	v_add_u32_e32 v71, 0x3000, v67
	v_lshlrev_b32_e32 v46, 1, v40
	v_lshlrev_b32_e32 v52, 1, v42
	v_mov_b32_e32 v53, v47
	v_lshlrev_b32_e32 v54, 1, v44
	v_mov_b32_e32 v55, v47
	v_lshlrev_b32_e32 v56, 1, v56
	v_mov_b32_e32 v57, v47
	s_mov_b32 s0, 0

_Z12scan2_kernelPKDF16_S0_S0_S0_S0_PKfS2_S2_S2_PDF16_PfS4_:
	s_and_b32 s3, s2, 7
	s_lshr_b32 s2, s2, 3
	s_lshl_b32 s3, s3, 5
	s_or_b32 s2, s2, s3
	s_ashr_i32 s4, s2, 31
	s_lshr_b32 s3, s4, 30
	s_lshr_b32 s4, s4, 25
	s_add_i32 s4, s2, s4
	s_add_i32 s3, s2, s3
	s_ashr_i32 s20, s4, 7
	v_readfirstlane_b32 s26, v0
	s_bfe_u32 s3, s3, 0x50002
	s_ashr_i32 s21, s20, 31
	s_lshr_b32 s25, s26, 6
	s_lshl_b64 s[34:35], s[20:21], 12
	s_lshl_b32 s4, s3, 7
	s_or_b32 s34, s34, s4
	s_sub_i32 s4, 11, s25
	s_cmpk_lt_u32 s26, 0x100
	s_load_dwordx8 s[12:19], s[0:1], 0x0
	s_cselect_b32 s27, s25, s4
	s_lshl_b32 s4, s2, 3
	s_and_b32 s28, s4, 24
	s_lshl_b32 s4, s20, 5
	s_or_b32 s22, s4, s3
	s_ashr_i32 s23, s22, 31
	s_lshl_b32 s29, s27, 4
	s_ashr_i32 s24, s27, 1
	s_lshl_b64 s[4:5], s[22:23], 15
	v_and_b32_e32 v1, 15, v0
	s_waitcnt lgkmcnt(0)
	s_add_u32 s4, s18, s4
	v_or_b32_e32 v90, s29, v1
	s_addc_u32 s5, s19, s5
	v_ashrrev_i32_e32 v91, 31, v90
	s_cmp_gt_i32 s24, 0
	v_lshlrev_b64 v[2:3], 8, v[90:91]
	s_cselect_b64 s[94:95], -1, 0
	v_and_b32_e32 v92, 48, v0
	v_mov_b32_e32 v93, 0
	v_lshl_add_u64 v[2:3], s[4:5], 0, v[2:3]
	s_mov_b32 s84, 0
	s_and_b64 s[4:5], s[94:95], exec
	v_lshl_add_u64 v[2:3], v[2:3], 0, v[92:93]
	s_cselect_b32 s4, 64, 0
	s_mov_b32 s5, s84
	s_cmp_lt_i32 s24, 2
	v_lshl_add_u64 v[4:5], v[2:3], 0, s[4:5]
	s_cselect_b32 s4, 0, 0x80
	s_cmp_lt_i32 s24, 3
	global_load_dwordx4 v[8:11], v[2:3], off
	global_load_dwordx4 v[12:15], v[4:5], off
	v_lshl_add_u64 v[4:5], v[2:3], 0, s[4:5]
	s_cselect_b32 s4, 0, 0xc0
	v_lshl_add_u64 v[2:3], v[2:3], 0, s[4:5]
	global_load_dwordx4 v[16:19], v[4:5], off
	global_load_dwordx4 v[32:35], v[2:3], off
	s_load_dwordx4 s[48:51], s[0:1], 0x40
	s_load_dwordx8 s[4:11], s[0:1], 0x20
	v_bfe_u32 v27, v0, 4, 2
	s_load_dwordx2 s[0:1], s[0:1], 0x50
	v_lshlrev_b32_e32 v26, 3, v27
	v_and_b32_e32 v23, 7, v0
	v_or_b32_e32 v29, 4, v26
	v_and_or_b32 v6, s29, 16, v1
	s_waitcnt lgkmcnt(0)
	v_writelane_b32 v239, s0, 0
	v_mov_b32_e32 v2, 0x3c00
	v_or_b32_e32 v30, 5, v26
	v_writelane_b32 v239, s1, 1
	s_and_b32 s0, s26, 0xffffff80
	s_cmpk_eq_i32 s0, 0x80
	v_or_b32_e32 v3, s28, v23
	v_cmp_eq_u32_e32 vcc, v29, v6
	s_cselect_b32 s29, s7, s9
	s_cselect_b32 s30, s6, s8
	s_lshl_b32 s8, s25, 10
	s_lshl_b32 s0, s28, 19
	v_lshlrev_b32_e32 v7, 2, v3
	v_cndmask_b32_e32 v3, 0, v2, vcc
	v_or_b32_e32 v31, 6, v26
	v_cmp_eq_u32_e32 vcc, v30, v6
	s_add_u32 s0, s14, s0
	s_addc_u32 s1, s15, 0
	v_cndmask_b32_e32 v4, 0, v2, vcc
	v_cmp_eq_u32_e32 vcc, v31, v6
	v_or_b32_e32 v28, 2, v26
	s_mul_hi_i32 s31, s20, 0x1200000
	v_cndmask_b32_e32 v5, 0, v2, vcc
	v_or_b32_e32 v25, 3, v26
	v_pack_b32_f16 v4, v3, v4
	v_lshrrev_b32_e32 v37, 3, v0
	v_or_b32_e32 v38, 0x200, v0
	v_lshrrev_b32_e32 v39, 3, v38
	v_lshlrev_b32_e32 v130, 12, v37
	v_and_b32_e32 v201, 63, v0
	v_lshlrev_b32_e32 v128, 12, v39
	v_lshlrev_b32_e32 v216, 4, v0
	s_mov_b64 s[54:55], s[50:51]
	v_or_b32_e32 v49, 0x60, v26
	v_or_b32_e32 v48, 0x46, v26
	v_or_b32_e32 v50, 0x65, v26
	v_or_b32_e32 v51, 0x64, v26
	v_or_b32_e32 v52, 0x63, v26
	v_or_b32_e32 v53, 0x62, v26
	v_or_b32_e32 v54, 0x67, v26
	v_lshlrev_b32_e32 v215, 4, v38
	v_mov_b32_e32 v127, v93
	v_mov_b32_e32 v131, v93
	v_mov_b32_e32 v129, v93
	s_mov_b32 s47, s84
	s_mov_b32 s65, 0x5040100
	v_mov_b32_e32 v234, v93
	s_mov_b32 s56, 0x41800000
	s_mov_b64 s[58:59], 0x8000
	s_mov_b64 s[82:83], 0x100
	s_waitcnt vmcnt(3)
	v_cvt_f32_f16_e32 v194, v8
	v_cvt_f32_f16_sdwa v94, v8 dst_sel:DWORD dst_unused:UNUSED_PAD src0_sel:WORD_1
	v_cvt_f32_f16_e32 v96, v9
	v_cvt_f32_f16_sdwa v97, v9 dst_sel:DWORD dst_unused:UNUSED_PAD src0_sel:WORD_1
	v_cvt_f32_f16_e32 v98, v10
	v_cvt_f32_f16_sdwa v99, v10 dst_sel:DWORD dst_unused:UNUSED_PAD src0_sel:WORD_1
	s_waitcnt vmcnt(0)
	v_cvt_f32_f16_e32 v197, v32
	v_cvt_f32_f16_sdwa v118, v32 dst_sel:DWORD dst_unused:UNUSED_PAD src0_sel:WORD_1
	v_cvt_f32_f16_e32 v120, v33
	v_cvt_f32_f16_sdwa v121, v33 dst_sel:DWORD dst_unused:UNUSED_PAD src0_sel:WORD_1
	v_or_b32_e32 v32, 7, v26
	global_load_dword v199, v7, s[48:49]
	global_load_dword v33, v7, s[10:11]
	s_mul_i32 s11, s20, 0x1200000
	v_cmp_eq_u32_e32 vcc, v32, v6
	s_add_u32 s0, s0, s11
	s_addc_u32 s1, s1, s31
	v_cndmask_b32_e32 v8, 0, v2, vcc
	v_cmp_eq_u32_e32 vcc, v28, v6
	s_lshl_b32 s46, s3, 8
	s_add_u32 s0, s0, s46
	v_cndmask_b32_e32 v3, 0, v2, vcc
	v_cmp_eq_u32_e32 vcc, v25, v6
	v_pack_b32_f16 v5, v5, v8
	v_or_b32_e32 v7, 1, v26
	v_cndmask_b32_e32 v8, 0, v2, vcc
	v_cmp_eq_u32_e32 vcc, v26, v6
	s_addc_u32 s1, s1, 0
	s_lshl_b64 s[6:7], s[22:23], 19
	v_pack_b32_f16 v3, v3, v8
	v_cndmask_b32_e32 v8, 0, v2, vcc
	v_cmp_eq_u32_e32 vcc, v7, v6
	v_lshl_add_u64 v[6:7], s[34:35], 0, v[90:91]
	s_add_u32 s22, s4, s6
	v_lshlrev_b64 v[6:7], 9, v[6:7]
	s_addc_u32 s23, s5, s7
	s_lshl_b32 s9, s28, 14
	v_lshl_add_u64 v[6:7], s[12:13], 0, v[6:7]
	s_add_u32 s4, s22, s9
	v_writelane_b32 v239, s34, 2
	v_cvt_f32_f16_e32 v122, v34
	v_cvt_f32_f16_sdwa v123, v34 dst_sel:DWORD dst_unused:UNUSED_PAD src0_sel:WORD_1
	v_cvt_f32_f16_e32 v124, v35
	v_cvt_f32_f16_sdwa v125, v35 dst_sel:DWORD dst_unused:UNUSED_PAD src0_sel:WORD_1
	v_lshl_add_u64 v[34:35], v[6:7], 0, v[92:93]
	v_lshrrev_b32_e32 v6, 4, v0
	s_addc_u32 s5, s23, 0
	v_writelane_b32 v239, s35, 3
	s_lshl_b64 s[12:13], s[34:35], 12
	v_xor_b32_e32 v7, v6, v0
	s_add_u32 s6, s16, s12
	v_writelane_b32 v239, s12, 4
	v_lshlrev_b32_e32 v7, 4, v7
	s_addc_u32 s7, s17, s13
	v_writelane_b32 v239, s13, 5
	s_lshl_b32 s12, s28, 6
	v_and_b32_e32 v7, 0xf0, v7
	v_writelane_b32 v239, s12, 6
	s_lshl_b32 s12, s28, 7
	v_lshl_or_b32 v92, v6, 13, v7
	v_lshl_or_b32 v22, v6, 8, v7
	v_xor_b32_e32 v6, v37, v0
	s_add_u32 s6, s6, s12
	v_lshlrev_b32_e32 v200, 4, v6
	v_lshrrev_b32_e32 v6, 4, v38
	s_addc_u32 s7, s7, 0
	s_lshl_b64 s[12:13], s[20:21], 19
	v_xor_b32_e32 v7, v6, v0
	s_add_u32 s18, s30, s12
	v_lshlrev_b32_e32 v7, 4, v7
	s_addc_u32 s19, s29, s13
	v_and_b32_e32 v7, 0xf0, v7
	s_add_u32 s9, s18, s9
	v_cndmask_b32_e32 v2, 0, v2, vcc
	v_lshl_or_b32 v126, v6, 13, v7
	v_lshl_or_b32 v24, v6, 8, v7
	v_xor_b32_e32 v6, v39, v0
	s_addc_u32 s18, s19, 0
	s_add_i32 s57, s8, 0
	v_cvt_f32_f16_e32 v100, v11
	v_cvt_f32_f16_sdwa v101, v11 dst_sel:DWORD dst_unused:UNUSED_PAD src0_sel:WORD_1
	v_cvt_f32_f16_e32 v195, v12
	v_cvt_f32_f16_sdwa v102, v12 dst_sel:DWORD dst_unused:UNUSED_PAD src0_sel:WORD_1
	v_cvt_f32_f16_e32 v104, v13
	v_cvt_f32_f16_sdwa v105, v13 dst_sel:DWORD dst_unused:UNUSED_PAD src0_sel:WORD_1
	v_cvt_f32_f16_e32 v106, v14
	v_cvt_f32_f16_sdwa v107, v14 dst_sel:DWORD dst_unused:UNUSED_PAD src0_sel:WORD_1
	v_cvt_f32_f16_e32 v108, v15
	v_cvt_f32_f16_sdwa v109, v15 dst_sel:DWORD dst_unused:UNUSED_PAD src0_sel:WORD_1
	v_cvt_f32_f16_e32 v196, v16
	v_cvt_f32_f16_sdwa v110, v16 dst_sel:DWORD dst_unused:UNUSED_PAD src0_sel:WORD_1
	v_cvt_f32_f16_e32 v112, v17
	v_cvt_f32_f16_sdwa v113, v17 dst_sel:DWORD dst_unused:UNUSED_PAD src0_sel:WORD_1
	v_cvt_f32_f16_e32 v114, v18
	v_cvt_f32_f16_sdwa v115, v18 dst_sel:DWORD dst_unused:UNUSED_PAD src0_sel:WORD_1
	v_cvt_f32_f16_e32 v116, v19
	v_cvt_f32_f16_sdwa v117, v19 dst_sel:DWORD dst_unused:UNUSED_PAD src0_sel:WORD_1
	v_pack_b32_f16 v2, v8, v2
	v_lshlrev_b32_e32 v198, 4, v6
	global_load_dwordx4 v[6:9], v[34:35], off offset:256
	global_load_dwordx4 v[10:13], v[34:35], off offset:320
	global_load_dwordx4 v[14:17], v[34:35], off offset:384
	global_load_dwordx4 v[18:21], v[34:35], off offset:448
	s_waitcnt vmcnt(0)
	s_add_i32 s8, s57, 0x4000
	s_mov_b32 m0, s57
	s_movk_i32 s10, 0x70
	s_add_i32 s19, s57, 0x8000
	global_load_lds_dwordx4 v92, s[0:1]
	s_mov_b32 m0, s8
	v_writelane_b32 v239, s8, 7
	global_load_lds_dwordx4 v22, s[4:5]
	v_and_or_b32 v34, v200, s10, v130
	s_mov_b32 m0, s19
	s_add_i32 s8, s57, 0x2000
	v_writelane_b32 v239, s19, 8
	global_load_lds_dwordx4 v34, s[6:7]
	s_mov_b32 m0, s8
	v_writelane_b32 v239, s8, 9
	global_load_lds_dwordx4 v126, s[0:1]
	s_add_i32 s0, s57, 0x6000
	v_writelane_b32 v239, s0, 10
	s_mov_b32 m0, s0
	s_add_i32 s0, s57, 0xa000
	v_and_or_b32 v35, s26, 64, v201
	s_lshl_b32 s25, s25, 8
	s_lshl_b32 s26, s3, 9
	global_load_lds_dwordx4 v24, s[4:5]
	v_writelane_b32 v239, s0, 11
	s_mov_b32 m0, s0
	s_add_u32 s0, s9, s26
	s_addc_u32 s1, s18, 0
	s_add_i32 s33, s25, 0
	v_and_or_b32 v36, v198, s10, v128
	s_add_i32 s4, s33, 0xc000
	global_load_lds_dwordx4 v36, s[6:7]
	v_lshlrev_b32_e32 v35, 2, v35
	s_mov_b32 m0, s4
	s_add_i32 s62, s57, 0x12800
	global_load_lds_dword v35, s[0:1]
	s_add_i32 s63, s57, 0x16800
	s_cmp_gt_i32 s24, -1
	s_cselect_b64 s[98:99], -1, 0
	s_cmp_lt_u32 s27, 2
	s_cselect_b64 s[96:97], -1, 0
	s_cmp_gt_u32 s27, 1
	s_cselect_b64 s[92:93], -1, 0
	s_cmp_eq_u32 s24, 1
	s_cselect_b64 s[88:89], -1, 0
	s_cmp_lg_u32 s24, 1
	s_cselect_b64 s[90:91], -1, 0
	s_cmp_gt_i32 s24, 1
	s_cselect_b64 s[34:35], -1, 0
	s_cmp_eq_u32 s24, 2
	v_writelane_b32 v239, s4, 12
	v_cmp_gt_i32_e64 s[0:1], v30, v90
	s_cselect_b64 s[36:37], -1, 0
	s_cmp_lg_u32 s24, 2
	v_writelane_b32 v239, s0, 13
	s_cselect_b64 s[38:39], -1, 0
	s_cmp_gt_i32 s24, 2
	v_writelane_b32 v239, s1, 14
	v_cmp_gt_i32_e64 s[0:1], v29, v90
	s_cselect_b64 s[40:41], -1, 0
	s_cmp_eq_u32 s24, 3
	v_writelane_b32 v239, s0, 15
	s_cselect_b64 s[42:43], -1, 0
	s_cmp_lg_u32 s24, 3
	v_writelane_b32 v239, s1, 16
	v_cmp_gt_i32_e64 s[4:5], v25, v90
	s_cselect_b64 s[44:45], -1, 0
	v_lshlrev_b32_e32 v25, 7, v90
	s_add_i32 s0, 0, 0x14800
	v_cmp_gt_i32_e64 s[6:7], v28, v90
	v_add_u32_e32 v28, s0, v25
	s_lshl_b64 s[18:19], s[20:21], 24
	s_lshl_b32 s0, s3, 19
	s_and_b32 s1, s2, 3
	s_or_b32 s0, s18, s0
	s_lshl_b32 s2, s1, 10
	s_add_i32 s64, 0, 0x19000
	s_or_b32 s18, s0, s2
	s_add_i32 s20, 0, 0x10800
	s_add_i32 s21, 0, 0x18800
	s_add_i32 s24, 0, 0x18a00
	s_lshl_b32 s0, s1, 22
	v_bfe_u32 v29, v0, 5, 1
	s_add_u32 s0, s11, s0
	v_cmp_gt_i32_e64 s[10:11], v31, v90
	v_bitop3_b32 v30, v29, v23, 2 bitop3:0x36
	v_bitop3_b32 v31, v29, v23, 4 bitop3:0x36
	v_bitop3_b32 v23, v29, v23, 6 bitop3:0x36
	v_bitop3_b32 v29, v29, v0, 7 bitop3:0x78
	v_cmp_gt_i32_e64 s[8:9], v32, v90
	v_lshlrev_b32_e32 v29, 4, v29
	v_lshlrev_b32_e32 v30, 4, v30
	v_lshlrev_b32_e32 v31, 4, v31
	v_lshlrev_b32_e32 v23, 4, v23
	v_add_u32_e32 v32, 0, v25
	v_add_u32_e32 v25, s64, v25
	v_add_u32_e32 v35, v32, v29
	v_add_u32_e32 v40, v32, v30
	v_add_u32_e32 v41, v32, v31
	v_add_u32_e32 v32, v32, v23
	v_add_u32_e32 v42, v25, v29
	v_add_u32_e32 v43, v25, v30
	v_add_u32_e32 v44, v25, v31
	v_add_u32_e32 v25, v25, v23
	v_add_u32_e32 v45, v28, v29
	v_add_u32_e32 v46, v28, v30
	v_add_u32_e32 v47, v28, v31
	v_add_u32_e32 v23, v28, v23
	v_bitop3_b32 v28, v37, 7, v0 bitop3:0x48
	v_bitop3_b32 v30, v39, 7, v0 bitop3:0x48
	v_bitop3_b32 v0, v27, v0, 15 bitop3:0x78
	v_lshlrev_b32_e32 v217, 4, v0
	v_bitop3_b32 v0, v27, v1, 4 bitop3:0x36
	v_lshlrev_b32_e32 v28, 4, v28
	v_lshlrev_b32_e32 v218, 4, v0
	v_bitop3_b32 v0, v27, v1, 8 bitop3:0x36
	s_addc_u32 s3, s31, 0
	s_or_b32 s0, s0, s46
	v_or3_b32 v28, s18, v130, v28
	v_mov_b32_e32 v29, s19
	v_lshlrev_b32_e32 v37, 4, v30
	v_lshlrev_b32_e32 v219, 4, v0
	v_lshlrev_b32_e32 v0, 8, v1
	v_bitop3_b32 v1, v27, v1, 12 bitop3:0x36
	s_add_u32 s2, s14, s0
	v_lshl_add_u64 v[30:31], s[50:51], 0, v[28:29]
	v_or3_b32 v28, s18, v128, v37
	v_and_b32_e32 v37, 8, v26
	v_lshlrev_b32_e32 v220, 4, v1
	v_lshlrev_b32_e32 v1, 5, v27
	s_addc_u32 s3, s15, s3
	s_lshl_b32 s46, s1, 17
	s_or_b32 s0, s12, s26
	s_and_b32 s25, s25, 0x100
	v_or_b32_e32 v27, 32, v26
	v_add_u32_e32 v221, 0, v0
	v_add_u32_e32 v222, s20, v0
	v_lshlrev_b32_e32 v0, 2, v90
	v_add_u32_e32 v209, v23, v37
	v_add_u32_e32 v210, v42, v37
	v_mov_b32_e32 v23, v93
	s_add_u32 s0, s30, s0
	v_or_b32_e32 v42, 64, v26
	v_add_u32_e32 v223, 0, v0
	v_add_u32_e32 v224, s21, v0
	v_lshlrev_b32_e32 v0, 2, v27
	v_writelane_b32 v239, s52, 17
	s_addc_u32 s1, s29, s13
	v_add_u32_e32 v228, s24, v0
	v_add_u32_e32 v229, s21, v0
	v_lshlrev_b32_e32 v0, 2, v42
	s_movk_i32 s48, 0xff80
	v_lshl_add_u64 v[132:133], s[22:23], 0, v[22:23]
	v_lshl_or_b32 v22, v201, 2, s25
	v_writelane_b32 v239, s53, 18
	v_add_u32_e32 v230, s24, v0
	v_add_u32_e32 v231, s21, v0
	v_lshlrev_b32_e32 v0, 2, v49
	s_mov_b32 s49, -1
	v_lshl_add_u64 v[136:137], s[0:1], 0, v[22:23]
	v_writelane_b32 v239, s54, 19
	v_lshl_add_u64 v[22:23], s[50:51], 0, v[28:29]
	v_add_u32_e32 v225, 0, v1
	v_add_u32_e32 v226, s24, v1
	v_add_u32_e32 v227, s21, v1
	v_add_u32_e32 v232, s24, v0
	v_add_u32_e32 v233, s21, v0
	v_lshl_add_u64 v[0:1], v[30:31], 0, s[48:49]
	v_writelane_b32 v239, s55, 20
	v_lshl_add_u64 v[142:143], v[22:23], 0, s[48:49]
	v_cmp_gt_i32_e64 s[48:49], v42, v90
	v_add_u32_e32 v211, v43, v37
	v_or_b32_e32 v43, 0x45, v26
	v_writelane_b32 v239, s48, 21
	v_add_u32_e32 v212, v44, v37
	v_or_b32_e32 v44, 0x44, v26
	v_writelane_b32 v239, s49, 22
	v_cmp_lt_i32_e64 s[48:49], v42, v90
	v_add_u32_e32 v206, v45, v37
	v_or_b32_e32 v45, 0x43, v26
	v_writelane_b32 v239, s48, 23
	v_add_u32_e32 v207, v46, v37
	v_or_b32_e32 v46, 0x42, v26
	v_writelane_b32 v239, s49, 24
	v_cmp_gt_i32_e64 s[48:49], v43, v90
	v_add_u32_e32 v208, v47, v37
	v_or_b32_e32 v47, 0x47, v26
	v_writelane_b32 v239, s48, 25
	v_add_u32_e32 v203, v40, v37
	v_add_u32_e32 v204, v41, v37
	v_writelane_b32 v239, s49, 26
	v_cmp_gt_i32_e64 s[48:49], v44, v90
	v_add_u32_e32 v205, v32, v37
	s_waitcnt vmcnt(0)
	v_mul_f32_e32 v214, 0x3d800000, v33
	v_writelane_b32 v239, s48, 27
	v_cmp_gt_i32_e64 s[12:13], v26, v90
	v_cmp_lt_i32_e64 s[14:15], v26, v90
	v_writelane_b32 v239, s49, 28
	v_cmp_gt_i32_e64 s[48:49], v45, v90
	v_or_b32_e32 v32, 37, v26
	v_or_b32_e32 v33, 36, v26
	v_writelane_b32 v239, s48, 29
	v_or_b32_e32 v38, 35, v26
	v_or_b32_e32 v39, 34, v26
	v_writelane_b32 v239, s49, 30
	v_cmp_gt_i32_e64 s[48:49], v46, v90
	v_or_b32_e32 v40, 39, v26
	v_or_b32_e32 v41, 38, v26
	v_writelane_b32 v239, s48, 31
	v_or_b32_e32 v26, 0x66, v26
	s_add_u32 s30, s16, s18
	v_writelane_b32 v239, s49, 32
	v_cmp_gt_i32_e64 s[48:49], v47, v90
	v_add_u32_e32 v202, v35, v37
	v_add_u32_e32 v213, v25, v37
	v_writelane_b32 v239, s48, 33
	v_mov_b32_e32 v35, v93
	v_mov_b32_e32 v25, v93
	v_writelane_b32 v239, s49, 34
	v_cmp_gt_i32_e64 s[48:49], v48, v90
	v_mov_b32_e32 v37, v93
	s_addc_u32 s31, s17, s19
	v_writelane_b32 v239, s48, 35
	v_cmp_gt_i32_e64 s[16:17], v27, v90
	v_cmp_lt_i32_e64 s[18:19], v27, v90
	v_writelane_b32 v239, s49, 36
	v_cmp_gt_i32_e64 s[48:49], v49, v90
	v_mov_b32_e32 v119, v120
	v_mov_b32_e32 v111, v112
	v_writelane_b32 v239, s48, 37
	v_mov_b32_e32 v103, v104
	v_mov_b32_e32 v95, v96
	v_writelane_b32 v239, s49, 38
	v_cmp_lt_i32_e64 s[48:49], v49, v90
	v_cmp_gt_i32_e64 s[20:21], v32, v90
	v_lshl_add_u64 v[134:135], s[22:23], 0, v[24:25]
	v_writelane_b32 v239, s48, 39
	v_cmp_gt_i32_e64 s[22:23], v33, v90
	v_cmp_gt_i32_e64 s[24:25], v38, v90
	v_writelane_b32 v239, s49, 40
	v_cmp_gt_i32_e64 s[48:49], v50, v90
	v_cmp_gt_i32_e64 s[26:27], v39, v90
	v_cmp_gt_i32_e64 s[28:29], v40, v90
	v_writelane_b32 v239, s48, 41
	v_lshl_add_u64 v[138:139], s[30:31], 0, v[34:35]
	v_lshl_add_u64 v[140:141], s[30:31], 0, v[36:37]
	v_writelane_b32 v239, s49, 42
	v_cmp_gt_i32_e64 s[48:49], v51, v90
	v_cmp_gt_i32_e64 s[30:31], v41, v90
	v_pk_mov_b32 v[144:145], v[120:121], v[122:123] op_sel:[1,0]
	v_writelane_b32 v239, s48, 43
	v_pk_mov_b32 v[146:147], v[122:123], v[124:125] op_sel:[1,0]
	v_pk_mov_b32 v[148:149], v[112:113], v[114:115] op_sel:[1,0]
	v_writelane_b32 v239, s49, 44
	v_cmp_gt_i32_e64 s[48:49], v52, v90
	v_pk_mov_b32 v[150:151], v[114:115], v[116:117] op_sel:[1,0]
	v_pk_mov_b32 v[152:153], v[104:105], v[106:107] op_sel:[1,0]
	v_writelane_b32 v239, s48, 45
	v_pk_mov_b32 v[154:155], v[106:107], v[108:109] op_sel:[1,0]
	v_pk_mov_b32 v[156:157], v[96:97], v[98:99] op_sel:[1,0]
	v_writelane_b32 v239, s49, 46
	v_cmp_gt_i32_e64 s[48:49], v53, v90
	v_pk_mov_b32 v[158:159], v[98:99], v[100:101] op_sel:[1,0]
	s_mov_b32 s0, 0
	v_writelane_b32 v239, s48, 47
	s_mov_b64 s[50:51], 0x80000
	s_mov_b64 s[52:53], 0x4000
	v_writelane_b32 v239, s49, 48
	v_cmp_gt_i32_e64 s[48:49], v54, v90
	s_mov_b64 s[54:55], 0x80
	s_nop 0
	v_writelane_b32 v239, s48, 49
	s_nop 1
	v_writelane_b32 v239, s49, 50
	v_cmp_gt_i32_e64 s[48:49], v26, v90
	s_nop 1
	v_writelane_b32 v239, s48, 51
	s_nop 1
	v_writelane_b32 v239, s49, 52
	s_mov_b64 s[48:49], 0
